# N1 MoE-combine gather: tokens with 3+ experts load four expert rows in one trip (two pairs in flight), same arithmetic order
# speedup vs baseline: 1.0005x; 1.0005x over previous
.LBB0_236:
	s_bcnt1_i32_b32 s100, s11
	s_cmp_lt_u32 s100, 3
	s_cbranch_scc1 .Lg4n1_orig
	s_ff1_i32_b32 s13, s11
	s_add_i32 s16, s11, -1
	s_and_b32 s11, s16, s11
	s_ff1_i32_b32 s20, s11
	s_add_i32 s16, s11, -1
	s_and_b32 s11, s16, s11
	s_ff1_i32_b32 s100, s11
	s_add_i32 s16, s11, -1
	s_and_b32 s11, s16, s11
	s_ff1_i32_b32 s101, s11
	s_cmp_eq_u32 s11, 0
	s_cselect_b32 s101, s100, s101
	s_cselect_b32 s21, 0, 1.0
	s_add_i32 s16, s11, -1
	s_and_b32 s11, s16, s11
	v_readlane_b32 s16, v135, s13
	s_nop 0
	s_ashr_i32 s17, s16, 31
	s_lshl_b64 s[18:19], s[16:17], 2
	s_add_u32 s18, s24, s18
	s_addc_u32 s19, s25, s19
	global_load_dword v34, v65, s[18:19]
	s_lshl_b64 s[16:17], s[16:17], 10
	v_lshl_add_u64 v[36:37], v[118:119], 0, s[16:17]
	v_readlane_b32 s16, v135, s20
	s_nop 0
	s_ashr_i32 s17, s16, 31
	s_lshl_b64 s[18:19], s[16:17], 2
	s_add_u32 s18, s24, s18
	s_addc_u32 s19, s25, s19
	global_load_dword v32, v65, s[18:19]
	s_lshl_b64 s[16:17], s[16:17], 10
	v_lshl_add_u64 v[38:39], v[118:119], 0, s[16:17]
	global_load_dword v33, v[36:37], off nt
	global_load_dword v35, v[38:39], off nt
	global_load_dword v46, v[36:37], off offset:256 nt
	global_load_dword v137, v[38:39], off offset:256 nt
	global_load_dword v144, v[36:37], off offset:512 nt
	global_load_dword v148, v[38:39], off offset:512 nt
	global_load_dword v152, v[36:37], off offset:768 nt
	global_load_dword v156, v[38:39], off offset:768 nt
	v_readlane_b32 s16, v135, s100
	s_nop 0
	s_ashr_i32 s17, s16, 31
	s_lshl_b64 s[18:19], s[16:17], 2
	s_add_u32 s18, s24, s18
	s_addc_u32 s19, s25, s19
	global_load_dword v230, v65, s[18:19]
	s_lshl_b64 s[16:17], s[16:17], 10
	v_lshl_add_u64 v[232:233], v[118:119], 0, s[16:17]
	v_readlane_b32 s16, v135, s101
	s_nop 0
	s_ashr_i32 s17, s16, 31
	s_lshl_b64 s[18:19], s[16:17], 2
	s_add_u32 s18, s24, s18
	s_addc_u32 s19, s25, s19
	global_load_dword v231, v65, s[18:19]
	s_lshl_b64 s[16:17], s[16:17], 10
	v_lshl_add_u64 v[234:235], v[118:119], 0, s[16:17]
	global_load_dword v222, v[232:233], off nt
	global_load_dword v223, v[234:235], off nt
	global_load_dword v224, v[232:233], off offset:256 nt
	global_load_dword v225, v[234:235], off offset:256 nt
	global_load_dword v226, v[232:233], off offset:512 nt
	global_load_dword v227, v[234:235], off offset:512 nt
	global_load_dword v228, v[232:233], off offset:768 nt
	global_load_dword v229, v[234:235], off offset:768 nt
	s_waitcnt vmcnt(10)
	v_mul_f32_e32 v34, 0x3d800000, v34
	v_mul_f32_e32 v32, 0x3d800000, v32
	v_cvt_pk_f32_fp8_e32 v[36:37], v33
	v_cvt_pk_f32_fp8_e32 v[40:41], v35
	v_cvt_pk_f32_fp8_sdwa v[42:43], v35 src0_sel:WORD_1
	v_cvt_pk_f32_fp8_e32 v[138:139], v137
	v_cvt_pk_f32_fp8_sdwa v[140:141], v137 src0_sel:WORD_1
	v_cvt_pk_f32_fp8_e32 v[146:147], v148
	v_cvt_pk_f32_fp8_e32 v[150:151], v152
	v_cvt_pk_f32_fp8_sdwa v[152:153], v152 src0_sel:WORD_1
	v_cvt_pk_f32_fp8_e32 v[154:155], v156
	v_cvt_pk_f32_fp8_sdwa v[156:157], v156 src0_sel:WORD_1
	v_cvt_pk_f32_fp8_sdwa v[148:149], v148 src0_sel:WORD_1
	v_cvt_pk_f32_fp8_sdwa v[38:39], v33 src0_sel:WORD_1
	v_cvt_pk_f32_fp8_e32 v[44:45], v46
	v_cvt_pk_f32_fp8_sdwa v[46:47], v46 src0_sel:WORD_1
	v_cvt_pk_f32_fp8_e32 v[142:143], v144
	v_cvt_pk_f32_fp8_sdwa v[144:145], v144 src0_sel:WORD_1
	v_mul_f32_e32 v158, v32, v156
	v_mov_b32_e32 v35, v32
	v_mov_b32_e32 v156, v153
	v_pk_mul_f32 v[40:41], v[32:33], v[40:41] op_sel_hi:[0,1]
	v_pk_mul_f32 v[42:43], v[32:33], v[42:43] op_sel_hi:[0,1]
	v_pk_mul_f32 v[138:139], v[32:33], v[138:139] op_sel_hi:[0,1]
	v_pk_mul_f32 v[140:141], v[32:33], v[140:141] op_sel_hi:[0,1]
	v_pk_mul_f32 v[146:147], v[32:33], v[146:147] op_sel_hi:[0,1]
	v_pk_mul_f32 v[148:149], v[32:33], v[148:149] op_sel_hi:[0,1]
	v_pk_mul_f32 v[154:155], v[32:33], v[154:155] op_sel_hi:[0,1]
	v_pk_mul_f32 v[32:33], v[34:35], v[156:157]
	v_mul_f32_e32 v152, v34, v152
	v_mov_b32_e32 v153, v32
	v_mov_b32_e32 v159, v33
	v_pk_fma_f32 v[32:33], v[34:35], v[36:37], v[40:41] op_sel_hi:[0,1,1]
	v_pk_fma_f32 v[36:37], v[34:35], v[38:39], v[42:43] op_sel_hi:[0,1,1]
	v_pk_fma_f32 v[38:39], v[34:35], v[44:45], v[138:139] op_sel_hi:[0,1,1]
	v_pk_fma_f32 v[40:41], v[34:35], v[46:47], v[140:141] op_sel_hi:[0,1,1]
	v_pk_fma_f32 v[42:43], v[34:35], v[142:143], v[146:147] op_sel_hi:[0,1,1]
	v_pk_fma_f32 v[44:45], v[34:35], v[144:145], v[148:149] op_sel_hi:[0,1,1]
	v_pk_fma_f32 v[34:35], v[34:35], v[150:151], v[154:155] op_sel_hi:[0,1,1]
	v_pk_add_f32 v[46:47], v[152:153], v[158:159]
	v_pk_add_f32 v[28:29], v[28:29], v[34:35]
	v_pk_add_f32 v[30:31], v[30:31], v[46:47]
	v_pk_add_f32 v[26:27], v[26:27], v[44:45]
	v_pk_add_f32 v[24:25], v[24:25], v[42:43]
	v_pk_add_f32 v[22:23], v[22:23], v[40:41]
	v_pk_add_f32 v[20:21], v[20:21], v[38:39]
	v_pk_add_f32 v[18:19], v[18:19], v[36:37]
	v_pk_add_f32 v[16:17], v[16:17], v[32:33]
	s_waitcnt vmcnt(0)
	v_mov_b32_e32 v34, v230
	v_mul_f32_e32 v32, s21, v231
	v_mov_b32_e32 v33, v222
	v_mov_b32_e32 v35, v223
	v_mov_b32_e32 v46, v224
	v_mov_b32_e32 v137, v225
	v_mov_b32_e32 v144, v226
	v_mov_b32_e32 v148, v227
	v_mov_b32_e32 v152, v228
	v_mov_b32_e32 v156, v229
	v_mul_f32_e32 v34, 0x3d800000, v34
	v_mul_f32_e32 v32, 0x3d800000, v32
	v_cvt_pk_f32_fp8_e32 v[36:37], v33
	v_cvt_pk_f32_fp8_e32 v[40:41], v35
	v_cvt_pk_f32_fp8_sdwa v[42:43], v35 src0_sel:WORD_1
	v_cvt_pk_f32_fp8_e32 v[138:139], v137
	v_cvt_pk_f32_fp8_sdwa v[140:141], v137 src0_sel:WORD_1
	v_cvt_pk_f32_fp8_e32 v[146:147], v148
	v_cvt_pk_f32_fp8_e32 v[150:151], v152
	v_cvt_pk_f32_fp8_sdwa v[152:153], v152 src0_sel:WORD_1
	v_cvt_pk_f32_fp8_e32 v[154:155], v156
	v_cvt_pk_f32_fp8_sdwa v[156:157], v156 src0_sel:WORD_1
	v_cvt_pk_f32_fp8_sdwa v[148:149], v148 src0_sel:WORD_1
	v_cvt_pk_f32_fp8_sdwa v[38:39], v33 src0_sel:WORD_1
	v_cvt_pk_f32_fp8_e32 v[44:45], v46
	v_cvt_pk_f32_fp8_sdwa v[46:47], v46 src0_sel:WORD_1
	v_cvt_pk_f32_fp8_e32 v[142:143], v144
	v_cvt_pk_f32_fp8_sdwa v[144:145], v144 src0_sel:WORD_1
	v_mul_f32_e32 v158, v32, v156
	v_mov_b32_e32 v35, v32
	v_mov_b32_e32 v156, v153
	v_pk_mul_f32 v[40:41], v[32:33], v[40:41] op_sel_hi:[0,1]
	v_pk_mul_f32 v[42:43], v[32:33], v[42:43] op_sel_hi:[0,1]
	v_pk_mul_f32 v[138:139], v[32:33], v[138:139] op_sel_hi:[0,1]
	v_pk_mul_f32 v[140:141], v[32:33], v[140:141] op_sel_hi:[0,1]
	v_pk_mul_f32 v[146:147], v[32:33], v[146:147] op_sel_hi:[0,1]
	v_pk_mul_f32 v[148:149], v[32:33], v[148:149] op_sel_hi:[0,1]
	v_pk_mul_f32 v[154:155], v[32:33], v[154:155] op_sel_hi:[0,1]
	v_pk_mul_f32 v[32:33], v[34:35], v[156:157]
	v_mul_f32_e32 v152, v34, v152
	v_mov_b32_e32 v153, v32
	v_mov_b32_e32 v159, v33
	v_pk_fma_f32 v[32:33], v[34:35], v[36:37], v[40:41] op_sel_hi:[0,1,1]
	v_pk_fma_f32 v[36:37], v[34:35], v[38:39], v[42:43] op_sel_hi:[0,1,1]
	v_pk_fma_f32 v[38:39], v[34:35], v[44:45], v[138:139] op_sel_hi:[0,1,1]
	v_pk_fma_f32 v[40:41], v[34:35], v[46:47], v[140:141] op_sel_hi:[0,1,1]
	v_pk_fma_f32 v[42:43], v[34:35], v[142:143], v[146:147] op_sel_hi:[0,1,1]
	v_pk_fma_f32 v[44:45], v[34:35], v[144:145], v[148:149] op_sel_hi:[0,1,1]
	v_pk_fma_f32 v[34:35], v[34:35], v[150:151], v[154:155] op_sel_hi:[0,1,1]
	v_pk_add_f32 v[46:47], v[152:153], v[158:159]
	v_pk_add_f32 v[28:29], v[28:29], v[34:35]
	v_pk_add_f32 v[30:31], v[30:31], v[46:47]
	v_pk_add_f32 v[26:27], v[26:27], v[44:45]
	v_pk_add_f32 v[24:25], v[24:25], v[42:43]
	v_pk_add_f32 v[22:23], v[22:23], v[40:41]
	v_pk_add_f32 v[20:21], v[20:21], v[38:39]
	v_pk_add_f32 v[18:19], v[18:19], v[36:37]
	v_pk_add_f32 v[16:17], v[16:17], v[32:33]
	s_cmp_lg_u32 s11, 0
	s_cbranch_scc0 .LBB0_239
	s_branch .LBB0_236
